# attention phase: cross-half exchanges (running max, q sum of squares, softmax denominator) done with v_permlane32_swap_b32 in registers instead of ds_bpermute_b32 through LDS; bit-identical
# baseline (speedup 1.0000x reference)
.LBB0_613:
	v_mov_b32_e32 v225, v143
	v_mov_b32_e32 v226, v143
	s_nop 1
	v_permlane32_swap_b32 v225, v226
	v_lshlrev_b64 v[66:67], 11, v[144:145]
	v_lshl_add_u64 v[66:67], s[40:41], 0, v[66:67]
	v_lshl_add_u64 v[66:67], v[66:67], 0, s[8:9]
	s_add_i32 s30, s30, s13
	s_waitcnt lgkmcnt(0)
	v_add_f32_e32 v68, v225, v226
	v_div_scale_f32 v69, s[14:15], v68, v68, 1.0
	v_rcp_f32_e32 v70, v69
	v_div_scale_f32 v71, vcc, 1.0, v68, 1.0
	s_add_i32 s18, s18, s19
	v_fma_f32 v72, -v69, v70, 1.0
	v_fmac_f32_e32 v70, v72, v70
	v_mul_f32_e32 v72, v71, v70
	v_fma_f32 v73, -v69, v72, v71
	v_fmac_f32_e32 v72, v73, v70
	v_fma_f32 v69, -v69, v72, v71
	v_div_fmas_f32 v69, v69, v70, v72
	v_div_fixup_f32 v68, v69, v68, 1.0
	v_mul_f32_e32 v50, v68, v50
	v_mul_f32_e32 v51, v68, v51
	v_med3_f32 v50, v50, s29, v187
	v_med3_f32 v51, v51, s29, v187
	v_mov_b32_e32 v69, v131
	v_cvt_pk_fp8_f32 v69, v50, v51
	v_mul_f32_e32 v52, v68, v52
	v_mul_f32_e32 v50, v68, v53
	v_med3_f32 v51, v52, s29, v187
	v_med3_f32 v50, v50, s29, v187
	v_cvt_pk_fp8_f32 v69, v51, v50 op_sel:[0,0,1]
	v_mul_f32_e32 v50, v68, v54
	v_mul_f32_e32 v51, v68, v55
	v_med3_f32 v50, v50, s29, v187
	v_med3_f32 v51, v51, s29, v187
	v_mov_b32_e32 v53, v131
	v_cvt_pk_fp8_f32 v53, v50, v51
	v_mul_f32_e32 v52, v68, v56
	v_mul_f32_e32 v50, v68, v57
	v_med3_f32 v51, v52, s29, v187
	v_med3_f32 v50, v50, s29, v187
	v_cvt_pk_fp8_f32 v53, v51, v50 op_sel:[0,0,1]
	v_mul_f32_e32 v50, v68, v58
	v_mul_f32_e32 v51, v68, v59
	v_med3_f32 v50, v50, s29, v187
	v_med3_f32 v51, v51, s29, v187
	v_mov_b32_e32 v54, v131
	v_cvt_pk_fp8_f32 v54, v50, v51
	v_mul_f32_e32 v52, v68, v60
	v_mul_f32_e32 v50, v68, v61
	v_med3_f32 v51, v52, s29, v187
	v_med3_f32 v50, v50, s29, v187
	v_cvt_pk_fp8_f32 v54, v51, v50 op_sel:[0,0,1]
	v_lshl_add_u64 v[50:51], v[66:67], 0, v[132:133]
	global_store_dword v[50:51], v69, off
	global_store_dword v[50:51], v53, off offset:8
	global_store_dword v[50:51], v54, off offset:16
	v_mul_f32_e32 v52, v68, v62
	v_mul_f32_e32 v53, v68, v63
	v_med3_f32 v52, v52, s29, v187
	v_med3_f32 v53, v53, s29, v187
	v_mov_b32_e32 v55, v131
	v_cvt_pk_fp8_f32 v55, v52, v53
	v_mul_f32_e32 v54, v68, v64
	v_mul_f32_e32 v52, v68, v65
	v_med3_f32 v53, v54, s29, v187
	v_med3_f32 v52, v52, s29, v187
	v_mul_f32_e32 v34, v68, v34
	v_mul_f32_e32 v35, v68, v35
	v_cvt_pk_fp8_f32 v55, v53, v52 op_sel:[0,0,1]
	v_med3_f32 v34, v34, s29, v187
	v_med3_f32 v35, v35, s29, v187
	v_mov_b32_e32 v52, v131
	v_cvt_pk_fp8_f32 v52, v34, v35
	v_mul_f32_e32 v36, v68, v36
	v_mul_f32_e32 v34, v68, v37
	v_med3_f32 v35, v36, s29, v187
	v_med3_f32 v34, v34, s29, v187
	v_cvt_pk_fp8_f32 v52, v35, v34 op_sel:[0,0,1]
	v_mul_f32_e32 v34, v68, v38
	v_mul_f32_e32 v35, v68, v39
	v_med3_f32 v34, v34, s29, v187
	v_med3_f32 v35, v35, s29, v187
	v_mov_b32_e32 v37, v131
	v_cvt_pk_fp8_f32 v37, v34, v35
	v_mul_f32_e32 v36, v68, v40
	v_mul_f32_e32 v34, v68, v41
	v_med3_f32 v35, v36, s29, v187
	v_med3_f32 v34, v34, s29, v187
	v_cvt_pk_fp8_f32 v37, v35, v34 op_sel:[0,0,1]
	v_mul_f32_e32 v34, v68, v42
	v_mul_f32_e32 v35, v68, v43
	v_med3_f32 v34, v34, s29, v187
	v_med3_f32 v35, v35, s29, v187
	v_mov_b32_e32 v38, v131
	v_cvt_pk_fp8_f32 v38, v34, v35
	v_mul_f32_e32 v36, v68, v44
	v_mul_f32_e32 v34, v68, v45
	v_med3_f32 v35, v36, s29, v187
	v_med3_f32 v34, v34, s29, v187
	v_cvt_pk_fp8_f32 v38, v35, v34 op_sel:[0,0,1]
	v_mul_f32_e32 v34, v68, v46
	v_mul_f32_e32 v35, v68, v47
	global_store_dword v[50:51], v55, off offset:24
	global_store_dword v[50:51], v52, off offset:32
	global_store_dword v[50:51], v37, off offset:40
	global_store_dword v[50:51], v38, off offset:48
	v_med3_f32 v34, v34, s29, v187
	v_med3_f32 v35, v35, s29, v187
	v_mov_b32_e32 v37, v131
	v_cvt_pk_fp8_f32 v37, v34, v35
	v_mul_f32_e32 v36, v68, v48
	v_mul_f32_e32 v34, v68, v49
	v_med3_f32 v35, v36, s29, v187
	v_med3_f32 v34, v34, s29, v187
	v_mul_f32_e32 v18, v68, v18
	v_mul_f32_e32 v19, v68, v19
	v_cvt_pk_fp8_f32 v37, v35, v34 op_sel:[0,0,1]
	v_med3_f32 v18, v18, s29, v187
	v_med3_f32 v19, v19, s29, v187
	v_mov_b32_e32 v34, v131
	v_cvt_pk_fp8_f32 v34, v18, v19
	v_mul_f32_e32 v20, v68, v20
	v_mul_f32_e32 v18, v68, v21
	v_med3_f32 v19, v20, s29, v187
	v_med3_f32 v18, v18, s29, v187
	v_cvt_pk_fp8_f32 v34, v19, v18 op_sel:[0,0,1]
	v_mul_f32_e32 v18, v68, v22
	v_mul_f32_e32 v19, v68, v23
	v_med3_f32 v18, v18, s29, v187
	v_med3_f32 v19, v19, s29, v187
	v_mov_b32_e32 v21, v131
	v_cvt_pk_fp8_f32 v21, v18, v19
	v_mul_f32_e32 v20, v68, v24
	v_mul_f32_e32 v18, v68, v25
	v_med3_f32 v19, v20, s29, v187
	v_med3_f32 v18, v18, s29, v187
	v_cvt_pk_fp8_f32 v21, v19, v18 op_sel:[0,0,1]
	v_mul_f32_e32 v18, v68, v26
	v_mul_f32_e32 v19, v68, v27
	v_med3_f32 v18, v18, s29, v187
	v_med3_f32 v19, v19, s29, v187
	v_mov_b32_e32 v22, v131
	v_cvt_pk_fp8_f32 v22, v18, v19
	v_mul_f32_e32 v20, v68, v28
	v_mul_f32_e32 v18, v68, v29
	v_med3_f32 v19, v20, s29, v187
	v_med3_f32 v18, v18, s29, v187
	v_cvt_pk_fp8_f32 v22, v19, v18 op_sel:[0,0,1]
	v_mul_f32_e32 v18, v68, v30
	v_mul_f32_e32 v19, v68, v31
	global_store_dword v[50:51], v37, off offset:56
	global_store_dword v[50:51], v34, off offset:64
	global_store_dword v[50:51], v21, off offset:72
	global_store_dword v[50:51], v22, off offset:80
	v_med3_f32 v18, v18, s29, v187
	v_med3_f32 v19, v19, s29, v187
	v_mov_b32_e32 v21, v131
	v_cvt_pk_fp8_f32 v21, v18, v19
	v_mul_f32_e32 v20, v68, v32
	v_mul_f32_e32 v18, v68, v33
	v_med3_f32 v19, v20, s29, v187
	v_med3_f32 v18, v18, s29, v187
	v_mul_f32_e32 v2, v68, v2
	v_mul_f32_e32 v3, v68, v3
	v_cvt_pk_fp8_f32 v21, v19, v18 op_sel:[0,0,1]
	v_med3_f32 v2, v2, s29, v187
	v_med3_f32 v3, v3, s29, v187
	v_mov_b32_e32 v18, v131
	v_cvt_pk_fp8_f32 v18, v2, v3
	v_mul_f32_e32 v4, v68, v4
	v_mul_f32_e32 v2, v68, v5
	v_med3_f32 v3, v4, s29, v187
	v_med3_f32 v2, v2, s29, v187
	v_cvt_pk_fp8_f32 v18, v3, v2 op_sel:[0,0,1]
	v_mul_f32_e32 v2, v68, v6
	v_mul_f32_e32 v3, v68, v7
	v_med3_f32 v2, v2, s29, v187
	v_med3_f32 v3, v3, s29, v187
	v_mov_b32_e32 v5, v131
	v_cvt_pk_fp8_f32 v5, v2, v3
	v_mul_f32_e32 v4, v68, v8
	v_mul_f32_e32 v2, v68, v9
	v_med3_f32 v3, v4, s29, v187
	v_med3_f32 v2, v2, s29, v187
	v_cvt_pk_fp8_f32 v5, v3, v2 op_sel:[0,0,1]
	v_mul_f32_e32 v2, v68, v10
	v_mul_f32_e32 v3, v68, v11
	v_med3_f32 v2, v2, s29, v187
	v_med3_f32 v3, v3, s29, v187
	v_mov_b32_e32 v6, v131
	v_cvt_pk_fp8_f32 v6, v2, v3
	v_mul_f32_e32 v4, v68, v12
	v_mul_f32_e32 v2, v68, v13
	v_med3_f32 v3, v4, s29, v187
	v_med3_f32 v2, v2, s29, v187
	v_cvt_pk_fp8_f32 v6, v3, v2 op_sel:[0,0,1]
	v_mul_f32_e32 v2, v68, v14
	v_mul_f32_e32 v3, v68, v15
	global_store_dword v[50:51], v21, off offset:88
	global_store_dword v[50:51], v18, off offset:96
	global_store_dword v[50:51], v5, off offset:104
	global_store_dword v[50:51], v6, off offset:112
	v_med3_f32 v2, v2, s29, v187
	v_med3_f32 v3, v3, s29, v187
	v_mov_b32_e32 v5, v131
	v_cvt_pk_fp8_f32 v5, v2, v3
	v_mul_f32_e32 v4, v68, v16
	v_mul_f32_e32 v2, v68, v17
	v_med3_f32 v3, v4, s29, v187
	v_med3_f32 v2, v2, s29, v187
	v_cvt_pk_fp8_f32 v5, v3, v2 op_sel:[0,0,1]
	s_cmpk_gt_i32 s30, 0x3ff
	global_store_dword v[50:51], v5, off offset:120
	s_cbranch_scc1 .LBB0_630
.LBB0_614:
	s_lshl_b32 s8, s30, 6
	s_and_b32 s33, s8, 0x1fc0
	s_bfe_u32 s23, s30, 0x20007
	s_sub_i32 s8, 0x80, s33
	s_lshl_b32 s0, s23, 8
	s_and_b32 s22, s18, 0x1fc0
	s_ashr_i32 s14, s30, 9
	s_waitcnt vmcnt(4)
	v_sub_co_u32_e32 v54, vcc, s33, v184
	s_ashr_i32 s15, s8, 6
	s_and_b64 s[8:9], vcc, exec
	s_cselect_b32 s31, s15, 0
	s_ashr_i32 s15, s14, 31
	s_lshl_b64 s[8:9], s[14:15], 13
	v_or_b32_e32 v2, s33, v155
	s_lshl_b32 s35, s23, 2
	v_mov_b64_e32 v[50:51], s[36:37]
	v_or_b32_e32 v144, s8, v2
	s_add_i32 s35, s35, s16
	v_mad_u64_u32 v[2:3], s[42:43], v144, s20, v[50:51]
	v_mad_i32_i24 v3, s9, v185, v3
	s_lshl_b32 s42, s35, 8
	s_mov_b32 s43, s1
	v_lshl_add_u64 v[2:3], v[2:3], 0, s[42:43]
	v_mov_b32_e32 v143, v131
	v_lshl_add_u64 v[52:53], v[2:3], 0, v[142:143]
	global_load_dwordx4 v[58:61], v[52:53], off offset:224
	global_load_dwordx4 v[66:69], v[52:53], off offset:192
	global_load_dwordx4 v[74:77], v[52:53], off offset:160
	global_load_dwordx4 v[98:101], v[52:53], off offset:128
	global_load_dwordx4 v[42:45], v[134:135], off offset:16
	global_load_dwordx4 v[46:49], v[134:135], off
	global_load_dwordx4 v[34:37], v[134:135], off offset:80
	global_load_dwordx4 v[38:41], v[134:135], off offset:64
	global_load_dwordx4 v[26:29], v[134:135], off offset:144
	global_load_dwordx4 v[30:33], v[134:135], off offset:128
	global_load_dwordx4 v[18:21], v[134:135], off offset:208
	global_load_dwordx4 v[22:25], v[134:135], off offset:192
	global_load_dwordx4 v[10:13], v[134:135], off offset:272
	global_load_dwordx4 v[14:17], v[134:135], off offset:256
	global_load_dwordx4 v[2:5], v[134:135], off offset:336
	global_load_dwordx4 v[6:9], v[134:135], off offset:320
	global_load_dwordx4 v[102:105], v[52:53], off offset:64
	global_load_dwordx4 v[106:109], v[52:53], off offset:96
	global_load_dwordx4 v[110:113], v[52:53], off
	global_load_dwordx4 v[116:119], v[52:53], off offset:32
	s_mul_i32 s15, s23, 0x1800
	s_sub_i32 s23, 0x2040, s33
	s_lshr_b32 s33, s23, 6
	s_lshl_b32 s23, s31, 6
	v_add_u32_e32 v55, s23, v54
	v_or_b32_e32 v54, v55, v154
	v_or_b32_e32 v56, v55, v161
	v_ashrrev_i32_e32 v55, 31, v54
	v_ashrrev_i32_e32 v57, 31, v56
	v_lshl_add_u64 v[54:55], s[8:9], 0, v[54:55]
	v_lshl_add_u64 v[56:57], s[8:9], 0, v[56:57]
	s_waitcnt vmcnt(22)
	v_mad_u64_u32 v[62:63], s[42:43], v54, s20, v[50:51]
	v_mad_u64_u32 v[50:51], s[42:43], v56, s20, v[50:51]
	v_mad_i32_i24 v63, v55, s20, v63
	v_mad_i32_i24 v51, v57, s20, v51
	v_lshl_add_u64 v[52:53], v[62:63], 0, s[0:1]
	v_mov_b32_e32 v141, v131
	v_lshl_add_u64 v[50:51], v[50:51], 0, s[0:1]
	v_lshl_add_u64 v[52:53], v[52:53], 0, s[2:3]
	v_lshl_add_u64 v[50:51], v[50:51], 0, s[2:3]
	v_lshl_add_u64 v[54:55], v[52:53], 0, v[130:131]
	v_lshl_add_u64 v[52:53], v[52:53], 0, v[140:141]
	s_mov_b32 m0, s21
	v_lshl_add_u64 v[56:57], v[50:51], 0, v[130:131]
	v_lshl_add_u64 v[50:51], v[50:51], 0, v[140:141]
	v_lshl_add_u64 v[52:53], v[52:53], 0, s[4:5]
	global_load_dwordx4 v[90:93], v[54:55], off
	global_load_dwordx4 v[94:97], v[56:57], off
	v_lshl_add_u64 v[50:51], v[50:51], 0, s[4:5]
	global_load_lds_dwordx4 v[52:53], off
	s_mov_b32 m0, s26
	s_lshl_b32 s8, s35, 7
	global_load_lds_dwordx4 v[50:51], off
	s_lshl_b32 s35, s35, 2
	v_readlane_b32 s60, v251, 11
	v_readlane_b32 s74, v251, 25
	v_readlane_b32 s75, v251, 26
	s_add_i32 s22, s22, s23
	v_mov_b32_e32 v145, s9
	s_mov_b32 s9, s1
	s_min_u32 s33, s33, 4
	v_mov_b32_e32 v143, v156
	v_readlane_b32 s61, v251, 12
	v_readlane_b32 s62, v251, 13
	v_readlane_b32 s63, v251, 14
	v_readlane_b32 s64, v251, 15
	v_readlane_b32 s65, v251, 16
	v_readlane_b32 s66, v251, 17
	v_readlane_b32 s67, v251, 18
	v_readlane_b32 s68, v251, 19
	v_readlane_b32 s69, v251, 20
	v_readlane_b32 s70, v251, 21
	v_readlane_b32 s71, v251, 22
	v_readlane_b32 s72, v251, 23
	v_readlane_b32 s73, v251, 24
	s_waitcnt vmcnt(0)
	v_lshlrev_b32_e32 v54, 16, v59
	v_and_b32_e32 v63, 0xffff0000, v67
	v_lshlrev_b32_e32 v62, 16, v67
	v_mul_f32_e32 v64, v63, v63
	v_and_b32_e32 v195, 0xffff0000, v105
	v_lshlrev_b32_e32 v114, 16, v109
	v_and_b32_e32 v115, 0xffff0000, v109
	v_and_b32_e32 v109, 0xffff0000, v104
	v_lshlrev_b32_e32 v188, 16, v108
	v_and_b32_e32 v189, 0xffff0000, v108
	v_lshlrev_b32_e32 v194, 16, v105
	v_lshlrev_b32_e32 v108, 16, v104
	v_mov_b32_e32 v148, v195
	v_mov_b32_e32 v149, v109
	v_mov_b32_e32 v104, v194
	v_mov_b32_e32 v105, v108
	v_pk_mul_f32 v[148:149], v[148:149], v[148:149]
	v_and_b32_e32 v197, 0xffff0000, v103
	v_and_b32_e32 v199, 0xffff0000, v102
	v_pk_fma_f32 v[104:105], v[104:105], v[104:105], v[148:149]
	v_lshlrev_b32_e32 v196, 16, v103
	v_lshlrev_b32_e32 v198, 16, v102
	v_mov_b32_e32 v148, v199
	v_mov_b32_e32 v149, v197
	v_pk_fma_f32 v[124:125], v[62:63], v[62:63], v[64:65] op_sel_hi:[1,1,0]
	v_and_b32_e32 v65, 0xffff0000, v66
	v_mov_b32_e32 v102, v198
	v_mov_b32_e32 v103, v196
	v_pk_mul_f32 v[148:149], v[148:149], v[148:149]
	v_lshlrev_b32_e32 v64, 16, v66
	v_mul_f32_e32 v66, v65, v65
	v_pk_fma_f32 v[102:103], v[102:103], v[102:103], v[148:149]
	v_and_b32_e32 v55, 0xffff0000, v59
	v_lshlrev_b32_e32 v56, 16, v58
	v_and_b32_e32 v57, 0xffff0000, v58
	v_lshlrev_b32_e32 v58, 16, v69
	v_and_b32_e32 v59, 0xffff0000, v69
	v_pk_fma_f32 v[126:127], v[64:65], v[64:65], v[66:67] op_sel_hi:[1,1,0]
	v_and_b32_e32 v67, 0xffff0000, v77
	v_and_b32_e32 v69, 0xffff0000, v76
	v_pk_add_f32 v[102:103], v[102:103], v[102:103] op_sel:[0,1] op_sel_hi:[1,0]
	v_lshlrev_b32_e32 v50, 16, v61
	v_and_b32_e32 v51, 0xffff0000, v61
	v_lshlrev_b32_e32 v52, 16, v60
	v_and_b32_e32 v53, 0xffff0000, v60
	v_lshlrev_b32_e32 v60, 16, v68
	v_and_b32_e32 v61, 0xffff0000, v68
	v_lshlrev_b32_e32 v66, 16, v77
	v_lshlrev_b32_e32 v68, 16, v76
	v_mov_b32_e32 v72, v67
	v_mov_b32_e32 v73, v69
	v_pk_add_f32 v[102:103], v[104:105], v[102:103] op_sel:[1,0] op_sel_hi:[0,1]
	v_mov_b32_e32 v70, v66
	v_mov_b32_e32 v71, v68
	v_pk_mul_f32 v[72:73], v[72:73], v[72:73]
	v_pk_add_f32 v[102:103], v[104:105], v[102:103]
	v_lshlrev_b32_e32 v202, 16, v119
	v_and_b32_e32 v203, 0xffff0000, v119
	v_lshlrev_b32_e32 v104, 16, v118
	v_and_b32_e32 v105, 0xffff0000, v118
	v_lshlrev_b32_e32 v118, 16, v117
	v_and_b32_e32 v119, 0xffff0000, v117
	v_and_b32_e32 v117, 0xffff0000, v113
	v_pk_fma_f32 v[76:77], v[70:71], v[70:71], v[72:73]
	v_and_b32_e32 v71, 0xffff0000, v75
	v_and_b32_e32 v73, 0xffff0000, v74
	v_lshlrev_b32_e32 v204, 16, v116
	v_and_b32_e32 v205, 0xffff0000, v116
	v_lshlrev_b32_e32 v116, 16, v113
	v_and_b32_e32 v207, 0xffff0000, v112
	v_mov_b32_e32 v148, v117
	v_mov_b32_e32 v149, v203
	v_lshlrev_b32_e32 v70, 16, v75
	v_lshlrev_b32_e32 v72, 16, v74
	v_mov_b32_e32 v78, v73
	v_mov_b32_e32 v79, v71
	v_lshlrev_b32_e32 v206, 16, v112
	v_lshlrev_b32_e32 v112, 16, v111
	v_and_b32_e32 v113, 0xffff0000, v111
	v_lshlrev_b32_e32 v208, 16, v110
	v_and_b32_e32 v209, 0xffff0000, v110
	v_mov_b32_e32 v110, v116
	v_mov_b32_e32 v111, v202
	v_pk_mul_f32 v[148:149], v[148:149], v[148:149]
	v_mov_b32_e32 v150, v207
	v_mov_b32_e32 v151, v105
	v_mov_b32_e32 v74, v72
	v_mov_b32_e32 v75, v70
	v_pk_mul_f32 v[78:79], v[78:79], v[78:79]
	v_pk_fma_f32 v[110:111], v[110:111], v[110:111], v[148:149]
	v_mov_b32_e32 v148, v206
	v_mov_b32_e32 v149, v104
	v_pk_mul_f32 v[150:151], v[150:151], v[150:151]
	v_mov_b32_e32 v152, v113
	v_mov_b32_e32 v153, v119
	v_pk_fma_f32 v[74:75], v[74:75], v[74:75], v[78:79]
	v_pk_fma_f32 v[148:149], v[148:149], v[148:149], v[150:151]
	v_mov_b32_e32 v150, v112
	v_mov_b32_e32 v151, v118
	v_pk_mul_f32 v[152:153], v[152:153], v[152:153]
	v_mov_b32_e32 v210, v209
	v_mov_b32_e32 v211, v205
	v_pk_add_f32 v[74:75], v[74:75], v[74:75] op_sel:[0,1] op_sel_hi:[1,0]
	v_pk_fma_f32 v[150:151], v[150:151], v[150:151], v[152:153]
	v_mov_b32_e32 v152, v208
	v_mov_b32_e32 v153, v204
	v_pk_mul_f32 v[210:211], v[210:211], v[210:211]
	v_pk_add_f32 v[74:75], v[76:77], v[74:75] op_sel:[1,0] op_sel_hi:[0,1]
	v_pk_fma_f32 v[152:153], v[152:153], v[152:153], v[210:211]
	v_pk_add_f32 v[128:129], v[76:77], v[74:75]
	v_and_b32_e32 v77, 0xffff0000, v100
	v_and_b32_e32 v191, 0xffff0000, v107
	v_and_b32_e32 v193, 0xffff0000, v106
	v_pk_add_f32 v[150:151], v[152:153], v[150:151]
	v_lshlrev_b32_e32 v76, 16, v100
	v_lshlrev_b32_e32 v78, 16, v99
	v_and_b32_e32 v79, 0xffff0000, v99
	v_lshlrev_b32_e32 v80, 16, v98
	v_and_b32_e32 v81, 0xffff0000, v98
	v_lshlrev_b32_e32 v190, 16, v107
	v_mul_f32_e32 v98, v191, v191
	v_lshlrev_b32_e32 v192, 16, v106
	v_mul_f32_e32 v106, v193, v193
	v_pk_add_f32 v[148:149], v[148:149], v[150:151]
	v_mov_b32_e32 v150, v115
	v_mov_b32_e32 v151, v77
	v_lshlrev_b32_e32 v74, 16, v101
	v_and_b32_e32 v75, 0xffff0000, v101
	v_pk_mul_f32 v[100:101], v[78:79], v[78:79]
	v_pk_fma_f32 v[98:99], v[190:191], v[190:191], v[98:99] op_sel_hi:[1,1,0]
	v_pk_fma_f32 v[106:107], v[192:193], v[192:193], v[106:107] op_sel_hi:[1,1,0]
	v_pk_add_f32 v[110:111], v[110:111], v[148:149]
	v_mov_b32_e32 v148, v114
	v_mov_b32_e32 v149, v76
	v_pk_mul_f32 v[150:151], v[150:151], v[150:151]
	v_mov_b32_e32 v152, v189
	v_mov_b32_e32 v153, v81
	v_pk_fma_f32 v[148:149], v[148:149], v[148:149], v[150:151]
	v_mov_b32_e32 v150, v188
	v_mov_b32_e32 v151, v80
	v_pk_mul_f32 v[152:153], v[152:153], v[152:153]
	v_mov_b32_e32 v107, v100
	v_mov_b32_e32 v99, v101
	v_pk_mul_f32 v[146:147], v[74:75], v[74:75]
	v_pk_add_f32 v[110:111], v[110:111], v[110:111] op_sel:[0,1] op_sel_hi:[1,0]
	v_pk_fma_f32 v[150:151], v[150:151], v[150:151], v[152:153]
	v_pk_add_f32 v[98:99], v[106:107], v[98:99]
	v_mov_b32_e32 v111, v146
	v_pk_add_f32 v[98:99], v[150:151], v[98:99]
	v_mov_b32_e32 v103, v147
	v_pk_add_f32 v[98:99], v[148:149], v[98:99]
	v_pk_add_f32 v[100:101], v[110:111], v[102:103]
	v_mov_b32_e32 v102, v59
	v_pk_add_f32 v[98:99], v[100:101], v[98:99]
	v_mov_b32_e32 v103, v53
	v_pk_mul_f32 v[120:121], v[50:51], v[50:51]
	v_pk_mul_f32 v[122:123], v[54:55], v[54:55]
	v_pk_add_f32 v[98:99], v[98:99], v[98:99] op_sel:[0,1] op_sel_hi:[1,0]
	v_mov_b32_e32 v100, v58
	v_mov_b32_e32 v101, v52
	v_pk_mul_f32 v[102:103], v[102:103], v[102:103]
	v_mov_b32_e32 v106, v61
	v_mov_b32_e32 v107, v57
	v_pk_fma_f32 v[100:101], v[100:101], v[100:101], v[102:103]
	v_mov_b32_e32 v102, v60
	v_mov_b32_e32 v103, v56
	v_pk_mul_f32 v[106:107], v[106:107], v[106:107]
	v_mov_b32_e32 v127, v122
	v_mov_b32_e32 v125, v123
	v_mov_b32_e32 v99, v120
	v_mov_b32_e32 v129, v121
	v_pk_fma_f32 v[102:103], v[102:103], v[102:103], v[106:107]
	v_pk_add_f32 v[106:107], v[126:127], v[124:125]
	v_pk_add_f32 v[98:99], v[98:99], v[128:129]
	global_load_dwordx4 v[122:125], v[134:135], off offset:400
	global_load_dwordx4 v[126:129], v[134:135], off offset:384
	global_load_dwordx4 v[146:149], v[134:135], off offset:464
	global_load_dwordx4 v[150:153], v[134:135], off offset:448
	v_pk_add_f32 v[102:103], v[102:103], v[106:107]
	s_nop 0
	v_pk_add_f32 v[100:101], v[100:101], v[102:103]
	s_nop 0
	v_pk_add_f32 v[98:99], v[98:99], v[100:101]
	s_nop 0
	v_add_f32_e32 v98, v98, v99
	v_mov_b32_e32 v225, v98
	v_mov_b32_e32 v226, v98
	s_nop 1
	v_permlane32_swap_b32 v225, v226
	s_waitcnt lgkmcnt(0)
	v_add_f32_e32 v98, v225, v226
	v_fmamk_f32 v98, v98, 0x3c000000, v183
	v_rsq_f32_e32 v98, v98
	s_nop 0
	v_mul_f32_e32 v210, 0x3e0293ee, v98
	v_pk_mul_f32 v[2:3], v[210:211], v[2:3] op_sel_hi:[0,1]
	v_pk_mul_f32 v[4:5], v[210:211], v[4:5] op_sel_hi:[0,1]
	v_pk_mul_f32 v[2:3], v[2:3], v[68:69]
	v_pk_mul_f32 v[38:39], v[210:211], v[38:39] op_sel_hi:[0,1]
	v_pk_mul_f32 v[6:7], v[210:211], v[6:7] op_sel_hi:[0,1]
	v_cvt_pk_bf16_f32 v120, v2, v3
	v_pk_mul_f32 v[2:3], v[4:5], v[66:67]
	v_pk_mul_f32 v[40:41], v[210:211], v[40:41] op_sel_hi:[0,1]
	v_pk_mul_f32 v[38:39], v[38:39], v[204:205]
	v_pk_mul_f32 v[8:9], v[210:211], v[8:9] op_sel_hi:[0,1]
	v_pk_mul_f32 v[6:7], v[6:7], v[72:73]
	v_cvt_pk_bf16_f32 v102, v38, v39
	v_pk_mul_f32 v[38:39], v[40:41], v[118:119]
	v_cvt_pk_bf16_f32 v118, v6, v7
	v_pk_mul_f32 v[6:7], v[8:9], v[70:71]
	v_pk_mul_f32 v[22:23], v[210:211], v[22:23] op_sel_hi:[0,1]
	v_pk_mul_f32 v[24:25], v[210:211], v[24:25] op_sel_hi:[0,1]
	v_pk_mul_f32 v[22:23], v[22:23], v[192:193]
	v_cvt_pk_bf16_f32 v121, v2, v3
	v_cvt_pk_bf16_f32 v110, v22, v23
	v_pk_mul_f32 v[22:23], v[24:25], v[190:191]
	v_cvt_pk_bf16_f32 v119, v6, v7
	v_pk_mul_f32 v[42:43], v[210:211], v[42:43] op_sel_hi:[0,1]
	v_pk_mul_f32 v[10:11], v[210:211], v[10:11] op_sel_hi:[0,1]
	v_pk_mul_f32 v[46:47], v[210:211], v[46:47] op_sel_hi:[0,1]
	v_pk_mul_f32 v[44:45], v[210:211], v[44:45] op_sel_hi:[0,1]
	v_pk_mul_f32 v[42:43], v[42:43], v[206:207]
	v_pk_mul_f32 v[18:19], v[210:211], v[18:19] op_sel_hi:[0,1]
	v_pk_mul_f32 v[14:15], v[210:211], v[14:15] op_sel_hi:[0,1]
	v_pk_mul_f32 v[12:13], v[210:211], v[12:13] op_sel_hi:[0,1]
	v_pk_mul_f32 v[10:11], v[10:11], v[76:77]
	v_pk_mul_f32 v[48:49], v[210:211], v[48:49] op_sel_hi:[0,1]
	v_pk_mul_f32 v[46:47], v[46:47], v[208:209]
	v_cvt_pk_bf16_f32 v100, v42, v43
	v_pk_mul_f32 v[42:43], v[44:45], v[116:117]
	v_pk_mul_f32 v[20:21], v[210:211], v[20:21] op_sel_hi:[0,1]
	v_pk_mul_f32 v[18:19], v[18:19], v[188:189]
	v_pk_mul_f32 v[16:17], v[210:211], v[16:17] op_sel_hi:[0,1]
	v_pk_mul_f32 v[14:15], v[14:15], v[80:81]
	v_cvt_pk_bf16_f32 v116, v10, v11
	v_pk_mul_f32 v[10:11], v[12:13], v[74:75]
	v_cvt_pk_bf16_f32 v98, v46, v47
	v_pk_mul_f32 v[46:47], v[48:49], v[112:113]
	v_cvt_pk_bf16_f32 v112, v18, v19
	v_pk_mul_f32 v[18:19], v[20:21], v[114:115]
	v_cvt_pk_bf16_f32 v114, v14, v15
	v_pk_mul_f32 v[14:15], v[16:17], v[78:79]
	v_cvt_pk_bf16_f32 v117, v10, v11
	v_cvt_pk_bf16_f32 v115, v14, v15
	v_and_b32_e32 v15, 0xffff0000, v90
	v_cvt_pk_bf16_f32 v113, v18, v19
	v_lshlrev_b32_e32 v14, 16, v90
	v_mov_b32_e32 v18, v15
	v_mov_b32_e32 v16, v14
	v_cvt_pk_bf16_f32 v111, v22, v23
	v_pk_mul_f32 v[34:35], v[210:211], v[34:35] op_sel_hi:[0,1]
	v_pk_mul_f32 v[30:31], v[210:211], v[30:31] op_sel_hi:[0,1]
	v_pk_mul_f32 v[26:27], v[210:211], v[26:27] op_sel_hi:[0,1]
	s_waitcnt vmcnt(3)
	v_pk_mul_f32 v[8:9], v[210:211], v[122:123] op_sel_hi:[0,1]
	s_waitcnt vmcnt(2)
	v_pk_mul_f32 v[4:5], v[210:211], v[126:127] op_sel_hi:[0,1]
	v_pk_mul_f32 v[4:5], v[4:5], v[64:65]
	v_pk_mul_f32 v[2:3], v[210:211], v[128:129] op_sel_hi:[0,1]
	v_cvt_pk_bf16_f32 v122, v4, v5
	s_waitcnt vmcnt(0)
	v_pk_mul_f32 v[4:5], v[210:211], v[150:151] op_sel_hi:[0,1]
	v_pk_mul_f32 v[4:5], v[4:5], v[56:57]
	v_pk_mul_f32 v[2:3], v[2:3], v[62:63]
	v_cvt_pk_bf16_f32 v126, v4, v5
	v_mov_b32_e32 v4, s35
	global_load_dword v24, v4, s[74:75]
	v_pk_mul_f32 v[6:7], v[210:211], v[124:125] op_sel_hi:[0,1]
	v_cvt_pk_bf16_f32 v123, v2, v3
	v_pk_mul_f32 v[2:3], v[8:9], v[60:61]
	v_pk_mul_f32 v[8:9], v[210:211], v[146:147] op_sel_hi:[0,1]
	v_cvt_pk_bf16_f32 v124, v2, v3
	v_pk_mul_f32 v[2:3], v[6:7], v[58:59]
	v_and_b32_e32 v5, 0xffff0000, v92
	v_cvt_pk_bf16_f32 v125, v2, v3
	v_pk_mul_f32 v[2:3], v[210:211], v[152:153] op_sel_hi:[0,1]
	v_pk_mul_f32 v[2:3], v[2:3], v[54:55]
	v_lshlrev_b32_e32 v4, 16, v92
	v_cvt_pk_bf16_f32 v127, v2, v3
	v_pk_mul_f32 v[2:3], v[8:9], v[52:53]
	v_and_b32_e32 v9, 0xffff0000, v93
	v_lshlrev_b32_e32 v8, 16, v93
	v_mov_b32_e32 v12, v9
	v_mov_b32_e32 v13, v5
	v_mov_b32_e32 v10, v8
	v_mov_b32_e32 v11, v4
	v_pk_mul_f32 v[12:13], v[12:13], v[12:13]
	v_pk_mul_f32 v[6:7], v[210:211], v[148:149] op_sel_hi:[0,1]
	v_pk_fma_f32 v[10:11], v[10:11], v[10:11], v[12:13]
	v_and_b32_e32 v13, 0xffff0000, v91
	v_lshlrev_b32_e32 v12, 16, v91
	v_mov_b32_e32 v19, v13
	v_mov_b32_e32 v17, v12
	v_pk_mul_f32 v[18:19], v[18:19], v[18:19]
	v_cvt_pk_bf16_f32 v128, v2, v3
	v_pk_fma_f32 v[16:17], v[16:17], v[16:17], v[18:19]
	v_pk_mul_f32 v[2:3], v[6:7], v[50:51]
	v_add_f32_e32 v16, v16, v17
	v_add_f32_e32 v11, v11, v16
	v_add_f32_e32 v10, v10, v11
	v_cvt_pk_bf16_f32 v129, v2, v3
	v_and_b32_e32 v19, 0xffff0000, v94
	v_add_f32_dpp v10, v10, v10 quad_perm:[1,0,3,2] row_mask:0xf bank_mask:0xf bound_ctrl:1
	v_lshlrev_b32_e32 v18, 16, v94
	v_mov_b32_e32 v22, v19
	v_add_f32_dpp v10, v10, v10 quad_perm:[2,3,0,1] row_mask:0xf bank_mask:0xf bound_ctrl:1
	v_mov_b32_e32 v20, v18
	v_pk_mul_f32 v[36:37], v[210:211], v[36:37] op_sel_hi:[0,1]
	v_add_f32_dpp v10, v10, v10 row_half_mirror row_mask:0xf bank_mask:0xf bound_ctrl:1
	v_pk_mul_f32 v[34:35], v[34:35], v[104:105]
	v_pk_mul_f32 v[32:33], v[210:211], v[32:33] op_sel_hi:[0,1]
	v_add_f32_dpp v10, v10, v10 row_mirror row_mask:0xf bank_mask:0xf bound_ctrl:1
	v_fmamk_f32 v10, v10, 0x3c000000, v183
	v_rsq_f32_e32 v10, v10
	v_pk_mul_f32 v[28:29], v[210:211], v[28:29] op_sel_hi:[0,1]
	v_pk_mul_f32 v[30:31], v[30:31], v[198:199]
	v_pk_mul_f32 v[26:27], v[26:27], v[108:109]
	v_pk_mul_f32 v[6:7], v[88:89], v[10:11] op_sel_hi:[1,0]
	v_pk_mul_f32 v[2:3], v[86:87], v[10:11] op_sel_hi:[1,0]
	v_pk_mul_f32 v[16:17], v[84:85], v[10:11] op_sel_hi:[1,0]
	v_pk_mul_f32 v[10:11], v[82:83], v[10:11] op_sel_hi:[1,0]
	v_pk_mul_f32 v[2:3], v[2:3], v[14:15]
	v_pk_mul_f32 v[6:7], v[6:7], v[12:13]
	v_cvt_pk_bf16_f32 v2, v2, v3
	v_cvt_pk_bf16_f32 v3, v6, v7
	v_pk_mul_f32 v[4:5], v[10:11], v[4:5]
	v_and_b32_e32 v7, 0xffff0000, v97
	v_and_b32_e32 v11, 0xffff0000, v96
	v_lshlrev_b32_e32 v6, 16, v97
	v_lshlrev_b32_e32 v10, 16, v96
	v_mov_b32_e32 v14, v7
	v_mov_b32_e32 v15, v11
	v_mov_b32_e32 v12, v6
	v_mov_b32_e32 v13, v10
	v_pk_mul_f32 v[14:15], v[14:15], v[14:15]
	v_cvt_pk_bf16_f32 v4, v4, v5
	v_pk_fma_f32 v[12:13], v[12:13], v[12:13], v[14:15]
	v_and_b32_e32 v15, 0xffff0000, v95
	v_lshlrev_b32_e32 v14, 16, v95
	v_mov_b32_e32 v23, v15
	v_mov_b32_e32 v21, v14
	v_pk_mul_f32 v[22:23], v[22:23], v[22:23]
	v_pk_mul_f32 v[8:9], v[16:17], v[8:9]
	v_pk_fma_f32 v[20:21], v[20:21], v[20:21], v[22:23]
	v_cvt_pk_bf16_f32 v104, v34, v35
	v_add_f32_e32 v5, v20, v21
	v_add_f32_e32 v5, v13, v5
	v_add_f32_e32 v5, v12, v5
	v_pk_mul_f32 v[34:35], v[36:37], v[202:203]
	v_cvt_pk_bf16_f32 v106, v30, v31
	v_add_f32_dpp v5, v5, v5 quad_perm:[1,0,3,2] row_mask:0xf bank_mask:0xf bound_ctrl:1
	v_pk_mul_f32 v[30:31], v[32:33], v[196:197]
	v_cvt_pk_bf16_f32 v108, v26, v27
	v_add_f32_dpp v5, v5, v5 quad_perm:[2,3,0,1] row_mask:0xf bank_mask:0xf bound_ctrl:1
	v_pk_mul_f32 v[26:27], v[28:29], v[194:195]
	v_mov_b32_e32 v50, v131
	v_add_f32_dpp v5, v5, v5 row_half_mirror row_mask:0xf bank_mask:0xf bound_ctrl:1
	v_mov_b32_e32 v51, v131
	v_cvt_pk_bf16_f32 v99, v46, v47
	v_add_f32_dpp v5, v5, v5 row_mirror row_mask:0xf bank_mask:0xf bound_ctrl:1
	v_fmamk_f32 v5, v5, 0x3c000000, v183
	v_rsq_f32_e32 v12, v5
	v_cvt_pk_bf16_f32 v5, v8, v9
	ds_write_b128 v157, v[2:5]
	v_cvt_pk_bf16_f32 v101, v42, v43
	v_pk_mul_f32 v[4:5], v[88:89], v[12:13] op_sel_hi:[1,0]
	v_pk_mul_f32 v[2:3], v[86:87], v[12:13] op_sel_hi:[1,0]
	v_pk_mul_f32 v[8:9], v[84:85], v[12:13] op_sel_hi:[1,0]
	v_pk_mul_f32 v[12:13], v[82:83], v[12:13] op_sel_hi:[1,0]
	v_pk_mul_f32 v[2:3], v[2:3], v[18:19]
	v_pk_mul_f32 v[4:5], v[4:5], v[14:15]
	v_cvt_pk_bf16_f32 v2, v2, v3
	v_cvt_pk_bf16_f32 v3, v4, v5
	v_pk_mul_f32 v[4:5], v[12:13], v[10:11]
	v_pk_mul_f32 v[6:7], v[8:9], v[6:7]
	v_cvt_pk_bf16_f32 v4, v4, v5
	v_cvt_pk_bf16_f32 v5, v6, v7
	v_add_u32_e32 v6, 0x2000, v157
	ds_write_b128 v6, v[2:5]
	v_add_u32_e32 v2, s22, v180
	v_mad_i64_i32 v[2:3], s[42:43], v2, s20, 0
	v_mad_i64_i32 v[2:3], s[42:43], s14, v186, v[2:3]
	v_lshl_add_u64 v[146:147], v[136:137], 0, v[2:3]
	v_lshl_add_u64 v[148:149], v[138:139], 0, v[2:3]
	v_add_u32_e32 v2, s22, v181
	v_mad_i64_i32 v[2:3], s[42:43], v2, s20, 0
	v_mad_i64_i32 v[2:3], s[42:43], s14, v186, v[2:3]
	s_lshl_b32 s14, s31, 8
	v_cvt_pk_bf16_f32 v103, v38, v39
	v_cvt_pk_bf16_f32 v105, v34, v35
	v_cvt_pk_bf16_f32 v107, v30, v31
	v_cvt_pk_bf16_f32 v109, v26, v27
	s_waitcnt vmcnt(0)
	v_mul_f32_e32 v188, 0x3fb8aa3b, v24
	v_lshl_add_u64 v[150:151], v[136:137], 0, v[2:3]
	v_lshl_add_u64 v[152:153], v[138:139], 0, v[2:3]
	s_add_i32 s15, s15, s14
	v_mov_b32_e32 v52, v131
	v_mov_b32_e32 v53, v131
	v_mov_b32_e32 v54, v131
	v_mov_b32_e32 v55, v131
	v_mov_b32_e32 v56, v131
	v_mov_b32_e32 v57, v131
	v_mov_b32_e32 v58, v131
	v_mov_b32_e32 v59, v131
	v_mov_b32_e32 v60, v131
	v_mov_b32_e32 v61, v131
	v_mov_b32_e32 v62, v131
	v_mov_b32_e32 v63, v131
	v_mov_b32_e32 v64, v131
	v_mov_b32_e32 v65, v131
	v_mov_b64_e32 v[34:35], v[50:51]
	v_mov_b64_e32 v[18:19], v[50:51]
	v_mov_b64_e32 v[2:3], v[50:51]
	s_or_b32 s35, s23, 63
	v_add_u32_e32 v141, s15, v182
	s_mov_b32 s42, s1
	v_mov_b64_e32 v[36:37], v[52:53]
	v_mov_b64_e32 v[38:39], v[54:55]
	v_mov_b64_e32 v[40:41], v[56:57]
	v_mov_b64_e32 v[42:43], v[58:59]
	v_mov_b64_e32 v[44:45], v[60:61]
	v_mov_b64_e32 v[46:47], v[62:63]
	v_mov_b64_e32 v[48:49], v[64:65]
	v_mov_b64_e32 v[20:21], v[52:53]
	v_mov_b64_e32 v[22:23], v[54:55]
	v_mov_b64_e32 v[24:25], v[56:57]
	v_mov_b64_e32 v[26:27], v[58:59]
	v_mov_b64_e32 v[28:29], v[60:61]
	v_mov_b64_e32 v[30:31], v[62:63]
	v_mov_b64_e32 v[32:33], v[64:65]
	v_mov_b64_e32 v[4:5], v[52:53]
	v_mov_b64_e32 v[6:7], v[54:55]
	v_mov_b64_e32 v[8:9], v[56:57]
	v_mov_b64_e32 v[10:11], v[58:59]
	v_mov_b64_e32 v[12:13], v[60:61]
	v_mov_b64_e32 v[14:15], v[62:63]
	v_mov_b64_e32 v[16:17], v[64:65]
	s_waitcnt lgkmcnt(0)
	s_barrier
	s_branch .LBB0_616

.LBB0_620:
	s_sub_i32 s23, s35, 63
	s_add_i32 s22, s43, 0
	s_sub_i32 s44, s35, 32
	s_cmp_lt_i32 s44, s10
	s_cselect_b64 s[44:45], -1, 0
	s_cmp_gt_i32 s23, s17
	s_cselect_b64 s[46:47], -1, 0
	v_add_u32_e32 v66, s22, v158
	s_or_b64 s[44:45], s[44:45], s[46:47]
	s_andn2_b64 vcc, exec, s[44:45]
	v_add_u32_e32 v196, v66, v163
	v_add_u32_e32 v195, v66, v164
	v_add_u32_e32 v194, v66, v165
	v_add_u32_e32 v193, v66, v166
	v_add_u32_e32 v192, v66, v167
	v_add_u32_e32 v191, v66, v168
	v_add_u32_e32 v190, v66, v169
	v_add_u32_e32 v189, v66, v170
	s_cbranch_vccz .LBB0_624
	ds_read_b128 v[66:69], v196
	ds_read_b128 v[202:205], v195
	s_waitcnt lgkmcnt(0)
	v_mfma_f32_32x32x16_bf16 v[66:81], v[66:69], v[98:101], 0
	v_mfma_f32_32x32x16_bf16 v[66:81], v[202:205], v[102:105], v[66:81]
	ds_read_b128 v[202:205], v194
	ds_read_b128 v[206:209], v193
	s_waitcnt lgkmcnt(0)
	v_mfma_f32_32x32x16_bf16 v[66:81], v[202:205], v[106:109], v[66:81]
	v_mfma_f32_32x32x16_bf16 v[66:81], v[206:209], v[110:113], v[66:81]
	ds_read_b128 v[202:205], v192
	ds_read_b128 v[206:209], v191
	s_waitcnt lgkmcnt(0)
	v_mfma_f32_32x32x16_bf16 v[66:81], v[202:205], v[114:117], v[66:81]
	v_mfma_f32_32x32x16_bf16 v[66:81], v[206:209], v[118:121], v[66:81]
	ds_read_b128 v[202:205], v190
	ds_read_b128 v[206:209], v189
	ds_read2_b32 v[198:199], v141 offset1:1
	ds_read2_b32 v[210:211], v141 offset0:2 offset1:3
	ds_read2_b32 v[212:213], v141 offset0:8 offset1:9
	ds_read2_b32 v[214:215], v141 offset0:10 offset1:11
	ds_read2_b32 v[216:217], v141 offset0:16 offset1:17
	ds_read2_b32 v[218:219], v141 offset0:18 offset1:19
	ds_read2_b32 v[220:221], v141 offset0:24 offset1:25
	ds_read2_b32 v[222:223], v141 offset0:26 offset1:27
	s_waitcnt lgkmcnt(0)
	v_mfma_f32_32x32x16_bf16 v[66:81], v[202:205], v[122:125], v[66:81]
	v_mfma_f32_32x32x16_bf16 v[66:81], v[206:209], v[126:129], v[66:81]
	s_nop 11
	v_add_f32_e32 v205, v66, v198
	v_add_f32_e32 v204, v67, v199
	v_add_f32_e32 v203, v68, v210
	v_add_f32_e32 v202, v69, v211
	v_add_f32_e32 v197, v73, v215
	v_add_f32_e32 v73, v74, v216
	v_max3_f32 v74, v205, s28, v204
	v_add_f32_e32 v201, v70, v212
	v_add_f32_e32 v199, v71, v213
	v_max3_f32 v74, v74, v203, v202
	v_add_f32_e32 v198, v72, v214
	v_max3_f32 v74, v74, v201, v199
	v_add_f32_e32 v72, v75, v217
	v_max3_f32 v74, v74, v198, v197
	v_add_f32_e32 v71, v76, v218
	v_add_f32_e32 v70, v77, v219
	v_max3_f32 v74, v74, v73, v72
	v_add_f32_e32 v69, v78, v220
	v_add_f32_e32 v68, v79, v221
	v_max3_f32 v74, v74, v71, v70
	v_add_f32_e32 v67, v80, v222
	v_add_f32_e32 v66, v81, v223
	v_max3_f32 v74, v74, v69, v68
	v_max3_f32 v74, v74, v67, v66
	v_mov_b32_e32 v225, v74
	v_mov_b32_e32 v226, v74
	s_nop 1
	v_permlane32_swap_b32 v225, v226
	s_waitcnt lgkmcnt(0)
	v_max_f32_e32 v74, v225, v226
	v_add_f32_e32 v75, 0x41000000, v188
	v_cmp_gt_f32_e32 vcc, v74, v75
	s_cbranch_vccz .LBB0_623
	v_max_f32_e32 v74, v74, v74
	v_max_f32_e32 v75, v188, v188
	v_max_f32_e32 v75, v75, v74
	v_sub_f32_e32 v74, v188, v75
	v_exp_f32_e32 v74, v74
	v_mov_b32_e32 v188, v75
	v_pk_mul_f32 v[64:65], v[74:75], v[64:65] op_sel_hi:[0,1]
	v_pk_mul_f32 v[62:63], v[74:75], v[62:63] op_sel_hi:[0,1]
	v_pk_mul_f32 v[60:61], v[74:75], v[60:61] op_sel_hi:[0,1]
	v_pk_mul_f32 v[58:59], v[74:75], v[58:59] op_sel_hi:[0,1]
	v_pk_mul_f32 v[56:57], v[74:75], v[56:57] op_sel_hi:[0,1]
	v_pk_mul_f32 v[54:55], v[74:75], v[54:55] op_sel_hi:[0,1]
	v_pk_mul_f32 v[52:53], v[74:75], v[52:53] op_sel_hi:[0,1]
	v_pk_mul_f32 v[50:51], v[74:75], v[50:51] op_sel_hi:[0,1]
	v_pk_mul_f32 v[48:49], v[74:75], v[48:49] op_sel_hi:[0,1]
	v_pk_mul_f32 v[46:47], v[74:75], v[46:47] op_sel_hi:[0,1]
	v_pk_mul_f32 v[44:45], v[74:75], v[44:45] op_sel_hi:[0,1]
	v_pk_mul_f32 v[42:43], v[74:75], v[42:43] op_sel_hi:[0,1]
	v_pk_mul_f32 v[40:41], v[74:75], v[40:41] op_sel_hi:[0,1]
	v_pk_mul_f32 v[38:39], v[74:75], v[38:39] op_sel_hi:[0,1]
	v_pk_mul_f32 v[36:37], v[74:75], v[36:37] op_sel_hi:[0,1]
	v_pk_mul_f32 v[34:35], v[74:75], v[34:35] op_sel_hi:[0,1]
	v_pk_mul_f32 v[32:33], v[74:75], v[32:33] op_sel_hi:[0,1]
	v_pk_mul_f32 v[30:31], v[74:75], v[30:31] op_sel_hi:[0,1]
	v_pk_mul_f32 v[28:29], v[74:75], v[28:29] op_sel_hi:[0,1]
	v_pk_mul_f32 v[26:27], v[74:75], v[26:27] op_sel_hi:[0,1]
	v_pk_mul_f32 v[24:25], v[74:75], v[24:25] op_sel_hi:[0,1]
	v_pk_mul_f32 v[22:23], v[74:75], v[22:23] op_sel_hi:[0,1]
	v_pk_mul_f32 v[20:21], v[74:75], v[20:21] op_sel_hi:[0,1]
	v_pk_mul_f32 v[18:19], v[74:75], v[18:19] op_sel_hi:[0,1]
	v_pk_mul_f32 v[16:17], v[74:75], v[16:17] op_sel_hi:[0,1]
	v_pk_mul_f32 v[14:15], v[74:75], v[14:15] op_sel_hi:[0,1]
	v_pk_mul_f32 v[12:13], v[74:75], v[12:13] op_sel_hi:[0,1]
	v_pk_mul_f32 v[10:11], v[74:75], v[10:11] op_sel_hi:[0,1]
	v_pk_mul_f32 v[8:9], v[74:75], v[8:9] op_sel_hi:[0,1]
	v_pk_mul_f32 v[6:7], v[74:75], v[6:7] op_sel_hi:[0,1]
	v_pk_mul_f32 v[4:5], v[74:75], v[4:5] op_sel_hi:[0,1]
	v_pk_mul_f32 v[2:3], v[74:75], v[2:3] op_sel_hi:[0,1]
	v_mul_f32_e32 v143, v143, v74

.LBB0_624:
	s_sub_i32 s23, s35, 31
	s_cmp_lt_i32 s35, s10
	s_cselect_b64 s[44:45], -1, 0
	s_cmp_gt_i32 s23, s17
	s_cselect_b64 s[46:47], -1, 0
	s_or_b64 s[44:45], s[44:45], s[46:47]
	s_and_b64 vcc, exec, s[44:45]
	s_cbranch_vccnz .LBB0_628
	ds_read_b128 v[66:69], v196 offset:8192
	ds_read_b128 v[196:199], v195 offset:8192
	s_waitcnt lgkmcnt(0)
	v_mfma_f32_32x32x16_bf16 v[66:81], v[66:69], v[98:101], 0
	v_mfma_f32_32x32x16_bf16 v[66:81], v[196:199], v[102:105], v[66:81]
	ds_read_b128 v[194:197], v194 offset:8192
	ds_read_b128 v[202:205], v193 offset:8192
	s_waitcnt lgkmcnt(0)
	v_mfma_f32_32x32x16_bf16 v[66:81], v[194:197], v[106:109], v[66:81]
	ds_read_b128 v[192:195], v192 offset:8192
	ds_read_b128 v[196:199], v191 offset:8192
	v_mfma_f32_32x32x16_bf16 v[66:81], v[202:205], v[110:113], v[66:81]
	s_waitcnt lgkmcnt(0)
	v_mfma_f32_32x32x16_bf16 v[66:81], v[192:195], v[114:117], v[66:81]
	v_mfma_f32_32x32x16_bf16 v[66:81], v[196:199], v[118:121], v[66:81]
	ds_read_b128 v[190:193], v190 offset:8192
	ds_read_b128 v[194:197], v189 offset:8192
	s_waitcnt lgkmcnt(0)
	v_mfma_f32_32x32x16_bf16 v[66:81], v[190:193], v[122:125], v[66:81]
	ds_read2_b32 v[190:191], v141 offset0:32 offset1:33
	ds_read2_b32 v[192:193], v141 offset0:34 offset1:35
	ds_read2_b32 v[198:199], v141 offset0:40 offset1:41
	ds_read2_b32 v[202:203], v141 offset0:42 offset1:43
	ds_read2_b32 v[204:205], v141 offset0:48 offset1:49
	ds_read2_b32 v[206:207], v141 offset0:50 offset1:51
	ds_read2_b32 v[208:209], v141 offset0:56 offset1:57
	ds_read2_b32 v[210:211], v141 offset0:58 offset1:59
	v_mfma_f32_32x32x16_bf16 v[66:81], v[194:197], v[126:129], v[66:81]
	s_waitcnt lgkmcnt(0)
	s_nop 10
	v_add_f32_e32 v196, v66, v190
	v_add_f32_e32 v195, v67, v191
	v_add_f32_e32 v194, v68, v192
	v_add_f32_e32 v193, v69, v193
	v_add_f32_e32 v189, v73, v203
	v_add_f32_e32 v73, v74, v204
	v_max3_f32 v74, v196, s28, v195
	v_add_f32_e32 v192, v70, v198
	v_add_f32_e32 v191, v71, v199
	v_max3_f32 v74, v74, v194, v193
	v_add_f32_e32 v190, v72, v202
	v_max3_f32 v74, v74, v192, v191
	v_add_f32_e32 v72, v75, v205
	v_max3_f32 v74, v74, v190, v189
	v_add_f32_e32 v71, v76, v206
	v_add_f32_e32 v70, v77, v207
	v_max3_f32 v74, v74, v73, v72
	v_add_f32_e32 v69, v78, v208
	v_add_f32_e32 v68, v79, v209
	v_max3_f32 v74, v74, v71, v70
	v_add_f32_e32 v67, v80, v210
	v_add_f32_e32 v66, v81, v211
	v_max3_f32 v74, v74, v69, v68
	v_max3_f32 v74, v74, v67, v66
	v_mov_b32_e32 v225, v74
	v_mov_b32_e32 v226, v74
	s_nop 1
	v_permlane32_swap_b32 v225, v226
	s_waitcnt lgkmcnt(0)
	v_max_f32_e32 v74, v225, v226
	v_add_f32_e32 v75, 0x41000000, v188
	v_cmp_gt_f32_e32 vcc, v74, v75
	s_cbranch_vccz .LBB0_627
	v_max_f32_e32 v74, v74, v74
	v_max_f32_e32 v75, v188, v188
	v_max_f32_e32 v75, v75, v74
	v_sub_f32_e32 v74, v188, v75
	v_exp_f32_e32 v74, v74
	v_mov_b32_e32 v188, v75
	v_pk_mul_f32 v[64:65], v[74:75], v[64:65] op_sel_hi:[0,1]
	v_pk_mul_f32 v[62:63], v[74:75], v[62:63] op_sel_hi:[0,1]
	v_pk_mul_f32 v[60:61], v[74:75], v[60:61] op_sel_hi:[0,1]
	v_pk_mul_f32 v[58:59], v[74:75], v[58:59] op_sel_hi:[0,1]
	v_pk_mul_f32 v[56:57], v[74:75], v[56:57] op_sel_hi:[0,1]
	v_pk_mul_f32 v[54:55], v[74:75], v[54:55] op_sel_hi:[0,1]
	v_pk_mul_f32 v[52:53], v[74:75], v[52:53] op_sel_hi:[0,1]
	v_pk_mul_f32 v[50:51], v[74:75], v[50:51] op_sel_hi:[0,1]
	v_pk_mul_f32 v[48:49], v[74:75], v[48:49] op_sel_hi:[0,1]
	v_pk_mul_f32 v[46:47], v[74:75], v[46:47] op_sel_hi:[0,1]
	v_pk_mul_f32 v[44:45], v[74:75], v[44:45] op_sel_hi:[0,1]
	v_pk_mul_f32 v[42:43], v[74:75], v[42:43] op_sel_hi:[0,1]
	v_pk_mul_f32 v[40:41], v[74:75], v[40:41] op_sel_hi:[0,1]
	v_pk_mul_f32 v[38:39], v[74:75], v[38:39] op_sel_hi:[0,1]
	v_pk_mul_f32 v[36:37], v[74:75], v[36:37] op_sel_hi:[0,1]
	v_pk_mul_f32 v[34:35], v[74:75], v[34:35] op_sel_hi:[0,1]
	v_pk_mul_f32 v[32:33], v[74:75], v[32:33] op_sel_hi:[0,1]
	v_pk_mul_f32 v[30:31], v[74:75], v[30:31] op_sel_hi:[0,1]
	v_pk_mul_f32 v[28:29], v[74:75], v[28:29] op_sel_hi:[0,1]
	v_pk_mul_f32 v[26:27], v[74:75], v[26:27] op_sel_hi:[0,1]
	v_pk_mul_f32 v[24:25], v[74:75], v[24:25] op_sel_hi:[0,1]
	v_pk_mul_f32 v[22:23], v[74:75], v[22:23] op_sel_hi:[0,1]
	v_pk_mul_f32 v[20:21], v[74:75], v[20:21] op_sel_hi:[0,1]
	v_pk_mul_f32 v[18:19], v[74:75], v[18:19] op_sel_hi:[0,1]
	v_pk_mul_f32 v[16:17], v[74:75], v[16:17] op_sel_hi:[0,1]
	v_pk_mul_f32 v[14:15], v[74:75], v[14:15] op_sel_hi:[0,1]
	v_pk_mul_f32 v[12:13], v[74:75], v[12:13] op_sel_hi:[0,1]
	v_pk_mul_f32 v[10:11], v[74:75], v[10:11] op_sel_hi:[0,1]
	v_pk_mul_f32 v[8:9], v[74:75], v[8:9] op_sel_hi:[0,1]
	v_pk_mul_f32 v[6:7], v[74:75], v[6:7] op_sel_hi:[0,1]
	v_pk_mul_f32 v[4:5], v[74:75], v[4:5] op_sel_hi:[0,1]
	v_pk_mul_f32 v[2:3], v[74:75], v[2:3] op_sel_hi:[0,1]
	v_mul_f32_e32 v143, v143, v74
